# k_g2 + MoE-up x8 folded into the w3 MFMA block scale (2^-3 instead of 2^-6, epilogue multiply removed) + q-up rope table loads hoisted
# baseline (speedup 1.0000x reference)
; #define PG8_STAGE(bufoff, gbase, voff) do { _Pragma("unroll") for (int _i = 0; _i < 2; ++_i) \
;         __builtin_amdgcn_global_load_lds((const unsigned*)((const char*)(gbase) + (voff)[_i]), (PG8_LAS unsigned*)(lds + (bufoff) + ldsw + _i * 8192), 16, 0, 0); } while (0)
; #define PG8_WAIT_V(n) asm volatile("s_waitcnt vmcnt(" #n ")" ::: "memory")
; #define PG8_WAIT_L(n) asm volatile("s_waitcnt lgkmcnt(" #n ")" ::: "memory")
; #define PG8_BAR __builtin_amdgcn_s_barrier()
; #define PG8_SCHED __builtin_amdgcn_sched_barrier(0)
; template <class Epi, class Sched, bool ALIGN_EPI = false, bool SP2 = false, bool F8 = false>
; __device__ __forceinline__ void gemm_phase(PG8_LAS unsigned char* lds, const Gemm g, const Sched& S, const Epi& E, const int tidb  ) {
;     ...
;             if constexpr (SP2) {
;             PG8_LDB(B0, 0, 0); PG8_LDB(B1, 0, 1); PG8_SCHED; PG8_LDA(At, 0, 0); PG8_STAGE(PG8_SA(1, 1), a1 + hstep, voffA);
;             PG8_WAIT_V(8); PG8_WAIT_L(0); PG8_BAR; PG8_MMA(0, 0, At, B0); PG8_MMA(0, 1, At, B1); PG8_BAR; PG8_SCHED;
;             PG8_LDA(At, 0, 1); PG8_STAGE(PG8_SB(0, 0), b2, voffB); PG8_STAGE(PG8_SB(0, 1), b2 + hstep, voffB); PG8_STAGE(PG8_SA(0, 0), a2, voffA);
;             PG8_WAIT_V(8); PG8_WAIT_L(0); PG8_BAR; PG8_MMA(1, 0, At, B0); PG8_MMA(1, 1, At, B1); PG8_BAR; PG8_SCHED;
.LBB0_1371:
	s_add_i32 s65, s24, 2
	s_add_u32 s67, s22, 0x80
	s_addc_u32 s25, s23, 0
	s_add_i32 s66, 0, 0x10000
	s_cmp_eq_u32 s57, s24
	s_cselect_b32 s25, s5, s25
	s_cselect_b32 s24, s4, s67
	v_add_u32_e32 v0, s66, v192
	s_cselect_b64 vcc, -1, 0
	s_add_i32 s67, 0, 0x14000
	ds_read_b128 v[18:21], v0
	ds_read_b128 v[22:25], v0 offset:1024
	ds_read_b128 v[26:29], v0 offset:2048
	ds_read_b128 v[30:33], v0 offset:3072
	v_add_u32_e32 v0, s67, v192
	ds_read_b128 v[2:5], v0
	ds_read_b128 v[6:9], v0 offset:1024
	ds_read_b128 v[10:13], v0 offset:2048
	ds_read_b128 v[14:17], v0 offset:3072
	v_cndmask_b32_e32 v189, v179, v177, vcc
	v_cndmask_b32_e32 v188, v178, v176, vcc
	v_lshl_add_u64 v[190:191], s[22:23], 0, v[172:173]
	s_add_i32 m0, s50, 0xc000
	ds_read_b128 v[180:183], v194
	ds_read_b128 v[184:187], v194 offset:1024
	ds_read_b128 v[204:207], v194 offset:2048
	ds_read_b128 v[208:211], v194 offset:3072
	ds_read_b128 v[212:215], v194 offset:4096
	ds_read_b128 v[216:219], v194 offset:5120
	ds_read_b128 v[220:223], v194 offset:6144
	ds_read_b128 v[224:227], v194 offset:7168
	global_load_lds_dwordx4 v[190:191], off
	v_lshl_add_u64 v[190:191], s[22:23], 0, v[174:175]
	s_add_i32 m0, s50, 0xe000
	s_nop 0
	global_load_lds_dwordx4 v[190:191], off
	s_waitcnt vmcnt(8)
	s_waitcnt lgkmcnt(0)
	s_barrier
	s_setprio 1
	s_waitcnt lgkmcnt(0)
	v_mfma_scale_f32_16x16x128_f8f6f4 v[154:157], v[18:25], v[180:187], v[154:157], v246, v253 op_sel_hi:[0,0,0]
	v_mfma_scale_f32_16x16x128_f8f6f4 v[150:153], v[26:33], v[180:187], v[150:153], v246, v253 op_sel_hi:[0,0,0]
	v_mfma_scale_f32_16x16x128_f8f6f4 v[142:145], v[18:25], v[204:211], v[142:145], v246, v253 op_sel_hi:[0,0,0]
	v_mfma_scale_f32_16x16x128_f8f6f4 v[134:137], v[26:33], v[204:211], v[134:137], v246, v253 op_sel_hi:[0,0,0]
	v_mfma_scale_f32_16x16x128_f8f6f4 v[126:129], v[18:25], v[212:219], v[126:129], v246, v253 op_sel_hi:[0,0,0]
	v_mfma_scale_f32_16x16x128_f8f6f4 v[118:121], v[26:33], v[212:219], v[118:121], v246, v253 op_sel_hi:[0,0,0]
	v_mfma_scale_f32_16x16x128_f8f6f4 v[110:113], v[18:25], v[220:227], v[110:113], v246, v253 op_sel_hi:[0,0,0]
	v_mfma_scale_f32_16x16x128_f8f6f4 v[102:105], v[26:33], v[220:227], v[102:105], v246, v253 op_sel_hi:[0,0,0]
	s_setprio 0
	s_setprio 1
	v_mfma_scale_f32_16x16x128_f8f6f4 v[158:161], v[2:9], v[180:187], v[158:161], v247, v253 op_sel_hi:[0,0,0]
	v_mfma_scale_f32_16x16x128_f8f6f4 v[146:149], v[10:17], v[180:187], v[146:149], v247, v253 op_sel_hi:[0,0,0]
	v_mfma_scale_f32_16x16x128_f8f6f4 v[138:141], v[2:9], v[204:211], v[138:141], v247, v253 op_sel_hi:[0,0,0]
	v_mfma_scale_f32_16x16x128_f8f6f4 v[130:133], v[10:17], v[204:211], v[130:133], v247, v253 op_sel_hi:[0,0,0]
	v_mfma_scale_f32_16x16x128_f8f6f4 v[122:125], v[2:9], v[212:219], v[122:125], v247, v253 op_sel_hi:[0,0,0]
	v_mfma_scale_f32_16x16x128_f8f6f4 v[114:117], v[10:17], v[212:219], v[114:117], v247, v253 op_sel_hi:[0,0,0]
	v_mfma_scale_f32_16x16x128_f8f6f4 v[106:109], v[2:9], v[220:227], v[106:109], v247, v253 op_sel_hi:[0,0,0]
	v_mfma_scale_f32_16x16x128_f8f6f4 v[98:101], v[10:17], v[220:227], v[98:101], v247, v253 op_sel_hi:[0,0,0]
	s_setprio 0
	s_barrier
	s_add_i32 s66, s66, s49
	v_lshl_add_u64 v[180:181], v[188:189], 0, v[166:167]
	s_mov_b32 m0, s66
	ds_read_b128 v[204:207], v194 offset:16384
	ds_read_b128 v[208:211], v194 offset:17408
	ds_read_b128 v[212:215], v194 offset:18432
	ds_read_b128 v[216:219], v194 offset:19456
	ds_read_b128 v[220:223], v194 offset:20480
	ds_read_b128 v[224:227], v194 offset:21504
	ds_read_b128 v[228:231], v194 offset:22528
	ds_read_b128 v[232:235], v194 offset:23552
	global_load_lds_dwordx4 v[180:181], off
	v_lshl_add_u64 v[182:183], v[188:189], 0, v[170:171]
	s_add_i32 m0, s66, 0x2000
	v_lshl_add_u64 v[186:187], v[188:189], 0, s[10:11]
	s_add_i32 s66, s67, s49
	global_load_lds_dwordx4 v[182:183], off
	v_lshl_add_u64 v[184:185], v[186:187], 0, v[166:167]
	s_mov_b32 m0, s66
	v_lshl_add_u64 v[186:187], v[186:187], 0, v[170:171]
	global_load_lds_dwordx4 v[184:185], off
	s_add_i32 m0, s66, 0x2000
	v_lshl_add_u64 v[188:189], s[24:25], 0, v[164:165]
	global_load_lds_dwordx4 v[186:187], off
	s_mov_b32 m0, s50
	v_lshl_add_u64 v[190:191], s[24:25], 0, v[168:169]
	global_load_lds_dwordx4 v[188:189], off
	s_mov_b32 m0, s51
	s_nop 0
	global_load_lds_dwordx4 v[190:191], off
	s_waitcnt vmcnt(8)
	s_waitcnt lgkmcnt(0)
	s_barrier
	s_setprio 1
	s_waitcnt lgkmcnt(0)
	v_mfma_scale_f32_16x16x128_f8f6f4 v[94:97], v[18:25], v[204:211], v[94:97], v246, v253 op_sel_hi:[0,0,0]
	v_mfma_scale_f32_16x16x128_f8f6f4 v[86:89], v[26:33], v[204:211], v[86:89], v246, v253 op_sel_hi:[0,0,0]
	v_mfma_scale_f32_16x16x128_f8f6f4 v[78:81], v[18:25], v[212:219], v[78:81], v246, v253 op_sel_hi:[0,0,0]
	v_mfma_scale_f32_16x16x128_f8f6f4 v[70:73], v[26:33], v[212:219], v[70:73], v246, v253 op_sel_hi:[0,0,0]
	v_mfma_scale_f32_16x16x128_f8f6f4 v[62:65], v[18:25], v[220:227], v[62:65], v246, v253 op_sel_hi:[0,0,0]
	v_mfma_scale_f32_16x16x128_f8f6f4 v[54:57], v[26:33], v[220:227], v[54:57], v246, v253 op_sel_hi:[0,0,0]
	v_mfma_scale_f32_16x16x128_f8f6f4 v[46:49], v[18:25], v[228:235], v[46:49], v246, v253 op_sel_hi:[0,0,0]
	v_mfma_scale_f32_16x16x128_f8f6f4 v[38:41], v[26:33], v[228:235], v[38:41], v246, v253 op_sel_hi:[0,0,0]
	s_setprio 0
	s_setprio 1
	v_mfma_scale_f32_16x16x128_f8f6f4 v[90:93], v[2:9], v[204:211], v[90:93], v247, v253 op_sel_hi:[0,0,0]
	v_mfma_scale_f32_16x16x128_f8f6f4 v[82:85], v[10:17], v[204:211], v[82:85], v247, v253 op_sel_hi:[0,0,0]
	v_mfma_scale_f32_16x16x128_f8f6f4 v[74:77], v[2:9], v[212:219], v[74:77], v247, v253 op_sel_hi:[0,0,0]
	v_mfma_scale_f32_16x16x128_f8f6f4 v[66:69], v[10:17], v[212:219], v[66:69], v247, v253 op_sel_hi:[0,0,0]
	v_mfma_scale_f32_16x16x128_f8f6f4 v[58:61], v[2:9], v[220:227], v[58:61], v247, v253 op_sel_hi:[0,0,0]
	v_mfma_scale_f32_16x16x128_f8f6f4 v[50:53], v[10:17], v[220:227], v[50:53], v247, v253 op_sel_hi:[0,0,0]
	v_mfma_scale_f32_16x16x128_f8f6f4 v[42:45], v[2:9], v[228:235], v[42:45], v247, v253 op_sel_hi:[0,0,0]
	v_mfma_scale_f32_16x16x128_f8f6f4 v[34:37], v[10:17], v[228:235], v[34:37], v247, v253 op_sel_hi:[0,0,0]
	s_setprio 0
	s_barrier
; #define PG8_STAGE(bufoff, gbase, voff) do { _Pragma("unroll") for (int _i = 0; _i < 2; ++_i) \
;         __builtin_amdgcn_global_load_lds((const unsigned*)((const char*)(gbase) + (voff)[_i]), (PG8_LAS unsigned*)(lds + (bufoff) + ldsw + _i * 8192), 16, 0, 0); } while (0)
; #define PG8_WAIT_V(n) asm volatile("s_waitcnt vmcnt(" #n ")" ::: "memory")
; #define PG8_WAIT_L(n) asm volatile("s_waitcnt lgkmcnt(" #n ")" ::: "memory")
; #define PG8_BAR __builtin_amdgcn_s_barrier()
; #define PG8_SCHED __builtin_amdgcn_sched_barrier(0)
; template <class Epi, class Sched, bool ALIGN_EPI = false, bool SP2 = false, bool F8 = false>
; __device__ __forceinline__ void gemm_phase(PG8_LAS unsigned char* lds, const Gemm g, const Sched& S, const Epi& E, const int tidb  ) {
;     ...
;         for (int t = 0; t < nt; t += 2) {
;             const bool last = (t == nt - 2);
;             if constexpr (Epi::PREFETCH) { if (t == 0) E.prefetch(cur, wid, lane); }
;             const char* a1 = cA + (size_t)(t + 1) * kstep;
;             const char* a2 = last ? nA : cA + (size_t)(t + 2) * kstep; const char* b2 = last ? nB : cB + (size_t)(t + 2) * kstep;
;             const char* a3 = a2 + kstep; const char* b3 = b2 + kstep;
;     ...
;             PG8_LDB(B0, 1, 0); PG8_LDB(B1, 1, 1); PG8_SCHED; PG8_LDA(At, 1, 0); PG8_STAGE(PG8_SA(0, 1), a2 + hstep, voffA);
;             PG8_WAIT_V(8); PG8_WAIT_L(0); PG8_BAR; PG8_MMA(0, 0, At, B0); PG8_MMA(0, 1, At, B1); PG8_BAR; PG8_SCHED;
;             PG8_LDA(At, 1, 1); PG8_STAGE(PG8_SB(1, 0), b3, voffB); PG8_STAGE(PG8_SB(1, 1), b3 + hstep, voffB); PG8_STAGE(PG8_SA(1, 0), a3, voffA);
;             PG8_WAIT_V(8); PG8_WAIT_L(0); PG8_BAR; PG8_MMA(1, 0, At, B0); PG8_MMA(1, 1, At, B1); PG8_BAR; PG8_SCHED;
	s_add_i32 s66, 0, 0x18000
	v_add_u32_e32 v0, s66, v192
	s_add_i32 s67, 0, 0x1c000
	ds_read_b128 v[2:5], v0
	ds_read_b128 v[6:9], v0 offset:1024
	ds_read_b128 v[10:13], v0 offset:2048
	ds_read_b128 v[14:17], v0 offset:3072
	v_add_u32_e32 v0, s67, v192
	ds_read_b128 v[18:21], v0
	ds_read_b128 v[22:25], v0 offset:1024
	ds_read_b128 v[26:29], v0 offset:2048
	ds_read_b128 v[30:33], v0 offset:3072
	s_add_u32 s24, s24, s10
	s_addc_u32 s25, s25, s11
	s_mov_b32 m0, s52
	v_lshl_add_u64 v[196:197], s[24:25], 0, v[164:165]
	ds_read_b128 v[204:207], v194 offset:32768
	ds_read_b128 v[208:211], v194 offset:33792
	ds_read_b128 v[212:215], v194 offset:34816
	ds_read_b128 v[216:219], v194 offset:35840
	ds_read_b128 v[220:223], v194 offset:36864
	ds_read_b128 v[224:227], v194 offset:37888
	ds_read_b128 v[228:231], v194 offset:38912
	ds_read_b128 v[232:235], v194 offset:39936
	global_load_lds_dwordx4 v[196:197], off
	v_lshl_add_u64 v[196:197], s[24:25], 0, v[168:169]
	s_mov_b32 m0, s53
	s_nop 0
	global_load_lds_dwordx4 v[196:197], off
	s_waitcnt vmcnt(8)
	s_waitcnt lgkmcnt(0)
	s_barrier
	s_setprio 1
	s_waitcnt lgkmcnt(0)
	v_mfma_scale_f32_16x16x128_f8f6f4 v[154:157], v[2:9], v[204:211], v[154:157], v246, v253 op_sel_hi:[0,0,0]
	v_mfma_scale_f32_16x16x128_f8f6f4 v[150:153], v[10:17], v[204:211], v[150:153], v246, v253 op_sel_hi:[0,0,0]
	v_mfma_scale_f32_16x16x128_f8f6f4 v[142:145], v[2:9], v[212:219], v[142:145], v246, v253 op_sel_hi:[0,0,0]
	v_mfma_scale_f32_16x16x128_f8f6f4 v[134:137], v[10:17], v[212:219], v[134:137], v246, v253 op_sel_hi:[0,0,0]
	v_mfma_scale_f32_16x16x128_f8f6f4 v[126:129], v[2:9], v[220:227], v[126:129], v246, v253 op_sel_hi:[0,0,0]
	v_mfma_scale_f32_16x16x128_f8f6f4 v[118:121], v[10:17], v[220:227], v[118:121], v246, v253 op_sel_hi:[0,0,0]
	v_mfma_scale_f32_16x16x128_f8f6f4 v[110:113], v[2:9], v[228:235], v[110:113], v246, v253 op_sel_hi:[0,0,0]
	v_mfma_scale_f32_16x16x128_f8f6f4 v[102:105], v[10:17], v[228:235], v[102:105], v246, v253 op_sel_hi:[0,0,0]
	s_setprio 0
	s_setprio 1
	v_mfma_scale_f32_16x16x128_f8f6f4 v[158:161], v[18:25], v[204:211], v[158:161], v247, v253 op_sel_hi:[0,0,0]
	v_mfma_scale_f32_16x16x128_f8f6f4 v[146:149], v[26:33], v[204:211], v[146:149], v247, v253 op_sel_hi:[0,0,0]
	v_mfma_scale_f32_16x16x128_f8f6f4 v[138:141], v[18:25], v[212:219], v[138:141], v247, v253 op_sel_hi:[0,0,0]
	v_mfma_scale_f32_16x16x128_f8f6f4 v[130:133], v[26:33], v[212:219], v[130:133], v247, v253 op_sel_hi:[0,0,0]
	v_mfma_scale_f32_16x16x128_f8f6f4 v[122:125], v[18:25], v[220:227], v[122:125], v247, v253 op_sel_hi:[0,0,0]
	v_mfma_scale_f32_16x16x128_f8f6f4 v[114:117], v[26:33], v[220:227], v[114:117], v247, v253 op_sel_hi:[0,0,0]
	v_mfma_scale_f32_16x16x128_f8f6f4 v[106:109], v[18:25], v[228:235], v[106:109], v247, v253 op_sel_hi:[0,0,0]
	v_mfma_scale_f32_16x16x128_f8f6f4 v[98:101], v[26:33], v[228:235], v[98:101], v247, v253 op_sel_hi:[0,0,0]
	s_setprio 0
	s_barrier
	s_add_i32 s24, s66, s49
	v_lshl_add_u64 v[180:181], v[180:181], 0, s[92:93]
	s_mov_b32 m0, s24
	ds_read_b128 v[204:207], v194 offset:49152
	ds_read_b128 v[208:211], v194 offset:50176
	ds_read_b128 v[212:215], v194 offset:51200
	ds_read_b128 v[216:219], v194 offset:52224
	ds_read_b128 v[220:223], v194 offset:53248
	ds_read_b128 v[224:227], v194 offset:54272
	ds_read_b128 v[228:231], v194 offset:55296
	ds_read_b128 v[232:235], v194 offset:56320
	global_load_lds_dwordx4 v[180:181], off
	v_lshl_add_u64 v[180:181], v[182:183], 0, s[92:93]
	s_add_i32 m0, s24, 0x2000
	s_add_i32 s24, s67, s49
	global_load_lds_dwordx4 v[180:181], off
	v_lshl_add_u64 v[180:181], v[184:185], 0, s[92:93]
	s_mov_b32 m0, s24
	s_nop 0
	global_load_lds_dwordx4 v[180:181], off
	v_lshl_add_u64 v[180:181], v[186:187], 0, s[92:93]
	s_add_i32 m0, s24, 0x2000
	s_nop 0
	global_load_lds_dwordx4 v[180:181], off
	v_lshl_add_u64 v[180:181], v[188:189], 0, s[92:93]
	s_mov_b32 m0, s54
	s_nop 0
	global_load_lds_dwordx4 v[180:181], off
	v_lshl_add_u64 v[180:181], v[190:191], 0, s[92:93]
	s_mov_b32 m0, s55
	s_nop 0
	global_load_lds_dwordx4 v[180:181], off
	s_waitcnt vmcnt(8)
	s_waitcnt lgkmcnt(0)
	s_barrier
	s_setprio 1
	s_waitcnt lgkmcnt(0)
	v_mfma_scale_f32_16x16x128_f8f6f4 v[94:97], v[2:9], v[204:211], v[94:97], v246, v253 op_sel_hi:[0,0,0]
	v_mfma_scale_f32_16x16x128_f8f6f4 v[86:89], v[10:17], v[204:211], v[86:89], v246, v253 op_sel_hi:[0,0,0]
	v_mfma_scale_f32_16x16x128_f8f6f4 v[78:81], v[2:9], v[212:219], v[78:81], v246, v253 op_sel_hi:[0,0,0]
	v_mfma_scale_f32_16x16x128_f8f6f4 v[70:73], v[10:17], v[212:219], v[70:73], v246, v253 op_sel_hi:[0,0,0]
	v_mfma_scale_f32_16x16x128_f8f6f4 v[62:65], v[2:9], v[220:227], v[62:65], v246, v253 op_sel_hi:[0,0,0]
	v_mfma_scale_f32_16x16x128_f8f6f4 v[54:57], v[10:17], v[220:227], v[54:57], v246, v253 op_sel_hi:[0,0,0]
	v_mfma_scale_f32_16x16x128_f8f6f4 v[46:49], v[2:9], v[228:235], v[46:49], v246, v253 op_sel_hi:[0,0,0]
	v_mfma_scale_f32_16x16x128_f8f6f4 v[38:41], v[10:17], v[228:235], v[38:41], v246, v253 op_sel_hi:[0,0,0]
	s_setprio 0
	s_setprio 1
	v_mfma_scale_f32_16x16x128_f8f6f4 v[90:93], v[18:25], v[204:211], v[90:93], v247, v253 op_sel_hi:[0,0,0]
	v_mfma_scale_f32_16x16x128_f8f6f4 v[82:85], v[26:33], v[204:211], v[82:85], v247, v253 op_sel_hi:[0,0,0]
	v_mfma_scale_f32_16x16x128_f8f6f4 v[74:77], v[18:25], v[212:219], v[74:77], v247, v253 op_sel_hi:[0,0,0]
	v_mfma_scale_f32_16x16x128_f8f6f4 v[66:69], v[26:33], v[212:219], v[66:69], v247, v253 op_sel_hi:[0,0,0]
	v_mfma_scale_f32_16x16x128_f8f6f4 v[58:61], v[18:25], v[220:227], v[58:61], v247, v253 op_sel_hi:[0,0,0]
	v_mfma_scale_f32_16x16x128_f8f6f4 v[50:53], v[26:33], v[220:227], v[50:53], v247, v253 op_sel_hi:[0,0,0]
	v_mfma_scale_f32_16x16x128_f8f6f4 v[42:45], v[18:25], v[228:235], v[42:45], v247, v253 op_sel_hi:[0,0,0]
	v_mfma_scale_f32_16x16x128_f8f6f4 v[34:37], v[26:33], v[228:235], v[34:37], v247, v253 op_sel_hi:[0,0,0]
	s_setprio 0
	s_barrier
	s_add_u32 s22, s22, 0x100
	s_addc_u32 s23, s23, 0
	v_lshl_add_u64 v[178:179], v[178:179], 0, s[84:85]
	s_cmp_ge_i32 s65, s56
	s_mov_b32 s24, s65
	s_cbranch_scc0 .LBB0_1371
	s_movk_i32 s67, 0x300

; __device__ __forceinline__ u32x4 pack8(const f32x4 a, const f32x4 b) { u32x4 w; w.x = cvt_pk_bf16(a[0], a[1]); w.y = cvt_pk_bf16(a[2], a[3]); w.z = cvt_pk_bf16(b[0], b[1]); w.w = cvt_pk_bf16(b[2], b[3]); return w; }
; __device__ __forceinline__ float silu_f(float x) { return x * __builtin_amdgcn_rcpf(1.0f + __builtin_amdgcn_exp2f(-1.4426950409f * x)); }
;     w = __builtin_amdgcn_cvt_pk_fp8_f32(__builtin_amdgcn_fmed3f(v[2] * 8.0f, -448.0f, 448.0f), __builtin_amdgcn_fmed3f(v[3] * 8.0f, -448.0f, 448.0f), w, true); return (unsigned)w; }
;     __device__ __forceinline__ void operator()(const f32x4 (&acc)[2][2][4][2], const Unit& u, int wr, int wc, int fr, int fq) const {
;     ...
;         const int row0 = u.pm * BM + wr * 64 + fr, col0 = u.pn * HALF + wc * 32 + 8 * fq;
; #pragma unroll
;         for (int ai = 0; ai < 2; ++ai)
; #pragma unroll
;             for (int m = 0; m < 4; ++m) {
;                 const float r = rs[ai][m]; f32x4 o[2];
; #pragma unroll
;                 for (int n = 0; n < 2; ++n) { const f32x4 a = acc[ai][0][m][n] * r, b = acc[ai][1][m][n] * r;
;                     o[n] = (f32x4){silu_f(a[0]) * b[0], silu_f(a[1]) * b[1], silu_f(a[2]) * b[2], silu_f(a[3]) * b[3]}; }
;                 if (F8OUT) { u32x2 w; w.x = pack4_fp8(o[0]); w.y = pack4_fp8(o[1]); *(u32x2*)((unsigned char*)h + (size_t)(row0 + ai * HALF + m * 16) * FFN + col0) = w; }
;                 else *(u32x4*)(h + (size_t)(row0 + ai * HALF + m * 16) * FFN + col0) = pack8(o[0], o[1]);
;             }
.LBB0_1375:
	v_mov_b32_e32 v14, 0xbfb8aa3b
	v_mov_b32_e32 v20, 1.0
	v_pk_mul_f32 v[4:5], v[154:155], v[14:15] op_sel_hi:[1,0]
	v_pk_mul_f32 v[6:7], v[156:157], v[14:15] op_sel_hi:[1,0]
	v_pk_mul_f32 v[8:9], v[150:151], v[14:15] op_sel_hi:[1,0]
	v_pk_mul_f32 v[10:11], v[152:153], v[14:15] op_sel_hi:[1,0]
	v_exp_f32_e32 v4, v4
	v_exp_f32_e32 v5, v5
	v_exp_f32_e32 v6, v6
	v_exp_f32_e32 v7, v7
	v_exp_f32_e32 v8, v8
	v_exp_f32_e32 v9, v9
	v_exp_f32_e32 v10, v10
	v_exp_f32_e32 v11, v11
	v_pk_add_f32 v[4:5], v[4:5], v[20:21] op_sel_hi:[1,0]
	v_pk_add_f32 v[6:7], v[6:7], v[20:21] op_sel_hi:[1,0]
	v_pk_add_f32 v[8:9], v[8:9], v[20:21] op_sel_hi:[1,0]
	v_pk_add_f32 v[10:11], v[10:11], v[20:21] op_sel_hi:[1,0]
	v_rcp_f32_e32 v4, v4
	v_rcp_f32_e32 v5, v5
	v_rcp_f32_e32 v6, v6
	v_rcp_f32_e32 v7, v7
	v_rcp_f32_e32 v8, v8
	v_rcp_f32_e32 v9, v9
	v_rcp_f32_e32 v10, v10
	v_rcp_f32_e32 v11, v11
	v_pk_mul_f32 v[4:5], v[154:155], v[4:5]
	v_pk_mul_f32 v[6:7], v[156:157], v[6:7]
	v_pk_mul_f32 v[8:9], v[150:151], v[8:9]
	v_pk_mul_f32 v[10:11], v[152:153], v[10:11]
	v_pk_mul_f32 v[4:5], v[158:159], v[4:5]
	v_pk_mul_f32 v[6:7], v[160:161], v[6:7]
	v_pk_mul_f32 v[8:9], v[146:147], v[8:9]
	v_pk_mul_f32 v[10:11], v[148:149], v[10:11]
	v_med3_f32 v4, v4, s64, v250
	v_med3_f32 v5, v5, s64, v250
	v_med3_f32 v6, v6, s64, v250
	v_med3_f32 v7, v7, s64, v250
	v_med3_f32 v8, v8, s64, v250
	v_med3_f32 v9, v9, s64, v250
	v_med3_f32 v10, v10, s64, v250
	v_med3_f32 v11, v11, s64, v250
	v_cvt_pk_fp8_f32 v12, v4, v5
	v_cvt_pk_fp8_f32 v13, v8, v9
	s_nop 0
	v_cvt_pk_fp8_f32 v12, v6, v7 op_sel:[0,0,1]
	v_cvt_pk_fp8_f32 v13, v10, v11 op_sel:[0,0,1]
	v_lshl_or_b32 v2, s62, 7, v193
	v_ashrrev_i32_e32 v3, 31, v2
	v_lshl_add_u32 v0, s63, 8, v163
	v_lshl_add_u64 v[2:3], s[20:21], 0, v[2:3]
	s_nop 15
	s_nop 15
	v_mad_i64_i32 v[18:19], s[22:23], v0, s73, v[2:3]
	s_waitcnt vmcnt(0)
	global_store_dwordx2 v[18:19], v[12:13], off
	v_pk_mul_f32 v[4:5], v[142:143], v[14:15] op_sel_hi:[1,0]
	v_pk_mul_f32 v[6:7], v[144:145], v[14:15] op_sel_hi:[1,0]
	v_pk_mul_f32 v[8:9], v[134:135], v[14:15] op_sel_hi:[1,0]
	v_pk_mul_f32 v[10:11], v[136:137], v[14:15] op_sel_hi:[1,0]
	v_exp_f32_e32 v4, v4
	v_exp_f32_e32 v5, v5
	v_exp_f32_e32 v6, v6
	v_exp_f32_e32 v7, v7
	v_exp_f32_e32 v8, v8
	v_exp_f32_e32 v9, v9
	v_exp_f32_e32 v10, v10
	v_exp_f32_e32 v11, v11
	v_pk_add_f32 v[4:5], v[4:5], v[20:21] op_sel_hi:[1,0]
	v_pk_add_f32 v[6:7], v[6:7], v[20:21] op_sel_hi:[1,0]
	v_pk_add_f32 v[8:9], v[8:9], v[20:21] op_sel_hi:[1,0]
	v_pk_add_f32 v[10:11], v[10:11], v[20:21] op_sel_hi:[1,0]
	v_rcp_f32_e32 v4, v4
	v_rcp_f32_e32 v5, v5
	v_rcp_f32_e32 v6, v6
	v_rcp_f32_e32 v7, v7
	v_rcp_f32_e32 v8, v8
	v_rcp_f32_e32 v9, v9
	v_rcp_f32_e32 v10, v10
	v_rcp_f32_e32 v11, v11
	v_pk_mul_f32 v[4:5], v[142:143], v[4:5]
	v_pk_mul_f32 v[6:7], v[144:145], v[6:7]
	v_pk_mul_f32 v[8:9], v[134:135], v[8:9]
	v_pk_mul_f32 v[10:11], v[136:137], v[10:11]
	v_pk_mul_f32 v[4:5], v[138:139], v[4:5]
	v_pk_mul_f32 v[6:7], v[140:141], v[6:7]
	v_pk_mul_f32 v[8:9], v[130:131], v[8:9]
	v_pk_mul_f32 v[10:11], v[132:133], v[10:11]
	v_med3_f32 v4, v4, s64, v250
	v_med3_f32 v5, v5, s64, v250
	v_med3_f32 v6, v6, s64, v250
	v_med3_f32 v7, v7, s64, v250
	v_med3_f32 v8, v8, s64, v250
	v_med3_f32 v9, v9, s64, v250
	v_med3_f32 v10, v10, s64, v250
	v_med3_f32 v11, v11, s64, v250
	v_cvt_pk_fp8_f32 v12, v4, v5
	v_cvt_pk_fp8_f32 v13, v8, v9
	s_nop 0
	v_cvt_pk_fp8_f32 v12, v6, v7 op_sel:[0,0,1]
	v_cvt_pk_fp8_f32 v13, v10, v11 op_sel:[0,0,1]
	v_or_b32_e32 v18, 16, v0
	v_mad_i64_i32 v[18:19], s[22:23], v18, s73, v[2:3]
	global_store_dwordx2 v[18:19], v[12:13], off
	v_pk_mul_f32 v[4:5], v[126:127], v[14:15] op_sel_hi:[1,0]
	v_pk_mul_f32 v[6:7], v[128:129], v[14:15] op_sel_hi:[1,0]
	v_pk_mul_f32 v[8:9], v[118:119], v[14:15] op_sel_hi:[1,0]
	v_pk_mul_f32 v[10:11], v[120:121], v[14:15] op_sel_hi:[1,0]
	v_exp_f32_e32 v4, v4
	v_exp_f32_e32 v5, v5
	v_exp_f32_e32 v6, v6
	v_exp_f32_e32 v7, v7
	v_exp_f32_e32 v8, v8
	v_exp_f32_e32 v9, v9
	v_exp_f32_e32 v10, v10
	v_exp_f32_e32 v11, v11
	v_pk_add_f32 v[4:5], v[4:5], v[20:21] op_sel_hi:[1,0]
	v_pk_add_f32 v[6:7], v[6:7], v[20:21] op_sel_hi:[1,0]
	v_pk_add_f32 v[8:9], v[8:9], v[20:21] op_sel_hi:[1,0]
	v_pk_add_f32 v[10:11], v[10:11], v[20:21] op_sel_hi:[1,0]
	v_rcp_f32_e32 v4, v4
	v_rcp_f32_e32 v5, v5
	v_rcp_f32_e32 v6, v6
	v_rcp_f32_e32 v7, v7
	v_rcp_f32_e32 v8, v8
	v_rcp_f32_e32 v9, v9
	v_rcp_f32_e32 v10, v10
	v_rcp_f32_e32 v11, v11
	v_pk_mul_f32 v[4:5], v[126:127], v[4:5]
	v_pk_mul_f32 v[6:7], v[128:129], v[6:7]
	v_pk_mul_f32 v[8:9], v[118:119], v[8:9]
	v_pk_mul_f32 v[10:11], v[120:121], v[10:11]
	v_pk_mul_f32 v[4:5], v[122:123], v[4:5]
	v_pk_mul_f32 v[6:7], v[124:125], v[6:7]
	v_pk_mul_f32 v[8:9], v[114:115], v[8:9]
	v_pk_mul_f32 v[10:11], v[116:117], v[10:11]
	v_med3_f32 v4, v4, s64, v250
	v_med3_f32 v5, v5, s64, v250
	v_med3_f32 v6, v6, s64, v250
	v_med3_f32 v7, v7, s64, v250
	v_med3_f32 v8, v8, s64, v250
	v_med3_f32 v9, v9, s64, v250
	v_med3_f32 v10, v10, s64, v250
	v_med3_f32 v11, v11, s64, v250
	v_cvt_pk_fp8_f32 v12, v4, v5
	v_cvt_pk_fp8_f32 v13, v8, v9
	s_nop 0
	v_cvt_pk_fp8_f32 v12, v6, v7 op_sel:[0,0,1]
	v_cvt_pk_fp8_f32 v13, v10, v11 op_sel:[0,0,1]
	v_or_b32_e32 v18, 32, v0
	v_mad_i64_i32 v[18:19], s[22:23], v18, s73, v[2:3]
	global_store_dwordx2 v[18:19], v[12:13], off
	v_pk_mul_f32 v[4:5], v[110:111], v[14:15] op_sel_hi:[1,0]
	v_pk_mul_f32 v[6:7], v[112:113], v[14:15] op_sel_hi:[1,0]
	v_pk_mul_f32 v[8:9], v[102:103], v[14:15] op_sel_hi:[1,0]
	v_pk_mul_f32 v[10:11], v[104:105], v[14:15] op_sel_hi:[1,0]
	v_exp_f32_e32 v4, v4
	v_exp_f32_e32 v5, v5
	v_exp_f32_e32 v6, v6
	v_exp_f32_e32 v7, v7
	v_exp_f32_e32 v8, v8
	v_exp_f32_e32 v9, v9
; __device__ __forceinline__ u32x4 pack8(const f32x4 a, const f32x4 b) { u32x4 w; w.x = cvt_pk_bf16(a[0], a[1]); w.y = cvt_pk_bf16(a[2], a[3]); w.z = cvt_pk_bf16(b[0], b[1]); w.w = cvt_pk_bf16(b[2], b[3]); return w; }
; __device__ __forceinline__ float silu_f(float x) { return x * __builtin_amdgcn_rcpf(1.0f + __builtin_amdgcn_exp2f(-1.4426950409f * x)); }
;     w = __builtin_amdgcn_cvt_pk_fp8_f32(__builtin_amdgcn_fmed3f(v[2] * 8.0f, -448.0f, 448.0f), __builtin_amdgcn_fmed3f(v[3] * 8.0f, -448.0f, 448.0f), w, true); return (unsigned)w; }
;     __device__ __forceinline__ void operator()(const f32x4 (&acc)[2][2][4][2], const Unit& u, int wr, int wc, int fr, int fq) const {
;     ...
;         const int row0 = u.pm * BM + wr * 64 + fr, col0 = u.pn * HALF + wc * 32 + 8 * fq;
; #pragma unroll
;         for (int ai = 0; ai < 2; ++ai)
; #pragma unroll
;             for (int m = 0; m < 4; ++m) {
;                 const float r = rs[ai][m]; f32x4 o[2];
; #pragma unroll
;                 for (int n = 0; n < 2; ++n) { const f32x4 a = acc[ai][0][m][n] * r, b = acc[ai][1][m][n] * r;
;                     o[n] = (f32x4){silu_f(a[0]) * b[0], silu_f(a[1]) * b[1], silu_f(a[2]) * b[2], silu_f(a[3]) * b[3]}; }
;                 if (F8OUT) { u32x2 w; w.x = pack4_fp8(o[0]); w.y = pack4_fp8(o[1]); *(u32x2*)((unsigned char*)h + (size_t)(row0 + ai * HALF + m * 16) * FFN + col0) = w; }
;                 else *(u32x4*)(h + (size_t)(row0 + ai * HALF + m * 16) * FFN + col0) = pack8(o[0], o[1]);
;             }
	v_exp_f32_e32 v10, v10
	v_exp_f32_e32 v11, v11
	v_pk_add_f32 v[4:5], v[4:5], v[20:21] op_sel_hi:[1,0]
	v_pk_add_f32 v[6:7], v[6:7], v[20:21] op_sel_hi:[1,0]
	v_pk_add_f32 v[8:9], v[8:9], v[20:21] op_sel_hi:[1,0]
	v_pk_add_f32 v[10:11], v[10:11], v[20:21] op_sel_hi:[1,0]
	v_rcp_f32_e32 v4, v4
	v_rcp_f32_e32 v5, v5
	v_rcp_f32_e32 v6, v6
	v_rcp_f32_e32 v7, v7
	v_rcp_f32_e32 v8, v8
	v_rcp_f32_e32 v9, v9
	v_rcp_f32_e32 v10, v10
	v_rcp_f32_e32 v11, v11
	v_pk_mul_f32 v[4:5], v[110:111], v[4:5]
	v_pk_mul_f32 v[6:7], v[112:113], v[6:7]
	v_pk_mul_f32 v[8:9], v[102:103], v[8:9]
	v_pk_mul_f32 v[10:11], v[104:105], v[10:11]
	v_pk_mul_f32 v[4:5], v[106:107], v[4:5]
	v_pk_mul_f32 v[6:7], v[108:109], v[6:7]
	v_pk_mul_f32 v[8:9], v[98:99], v[8:9]
	v_pk_mul_f32 v[10:11], v[100:101], v[10:11]
	v_med3_f32 v4, v4, s64, v250
	v_med3_f32 v5, v5, s64, v250
	v_med3_f32 v6, v6, s64, v250
	v_med3_f32 v7, v7, s64, v250
	v_med3_f32 v8, v8, s64, v250
	v_med3_f32 v9, v9, s64, v250
	v_med3_f32 v10, v10, s64, v250
	v_med3_f32 v11, v11, s64, v250
	v_cvt_pk_fp8_f32 v12, v4, v5
	v_cvt_pk_fp8_f32 v13, v8, v9
	s_nop 0
	v_cvt_pk_fp8_f32 v12, v6, v7 op_sel:[0,0,1]
	v_cvt_pk_fp8_f32 v13, v10, v11 op_sel:[0,0,1]
	v_or_b32_e32 v18, 48, v0
	v_mad_i64_i32 v[18:19], s[22:23], v18, s73, v[2:3]
	global_store_dwordx2 v[18:19], v[12:13], off
	v_pk_mul_f32 v[4:5], v[94:95], v[14:15] op_sel_hi:[1,0]
	v_pk_mul_f32 v[6:7], v[96:97], v[14:15] op_sel_hi:[1,0]
	v_pk_mul_f32 v[8:9], v[86:87], v[14:15] op_sel_hi:[1,0]
	v_pk_mul_f32 v[10:11], v[88:89], v[14:15] op_sel_hi:[1,0]
	v_exp_f32_e32 v4, v4
	v_exp_f32_e32 v5, v5
	v_exp_f32_e32 v6, v6
	v_exp_f32_e32 v7, v7
	v_exp_f32_e32 v8, v8
	v_exp_f32_e32 v9, v9
	v_exp_f32_e32 v10, v10
	v_exp_f32_e32 v11, v11
	v_pk_add_f32 v[4:5], v[4:5], v[20:21] op_sel_hi:[1,0]
	v_pk_add_f32 v[6:7], v[6:7], v[20:21] op_sel_hi:[1,0]
	v_pk_add_f32 v[8:9], v[8:9], v[20:21] op_sel_hi:[1,0]
	v_pk_add_f32 v[10:11], v[10:11], v[20:21] op_sel_hi:[1,0]
	v_rcp_f32_e32 v4, v4
	v_rcp_f32_e32 v5, v5
	v_rcp_f32_e32 v6, v6
	v_rcp_f32_e32 v7, v7
	v_rcp_f32_e32 v8, v8
	v_rcp_f32_e32 v9, v9
	v_rcp_f32_e32 v10, v10
	v_rcp_f32_e32 v11, v11
	v_pk_mul_f32 v[4:5], v[94:95], v[4:5]
	v_pk_mul_f32 v[6:7], v[96:97], v[6:7]
	v_pk_mul_f32 v[8:9], v[86:87], v[8:9]
	v_pk_mul_f32 v[10:11], v[88:89], v[10:11]
	v_pk_mul_f32 v[4:5], v[90:91], v[4:5]
	v_pk_mul_f32 v[6:7], v[92:93], v[6:7]
	v_pk_mul_f32 v[8:9], v[82:83], v[8:9]
	v_pk_mul_f32 v[10:11], v[84:85], v[10:11]
	v_med3_f32 v4, v4, s64, v250
	v_med3_f32 v5, v5, s64, v250
	v_med3_f32 v6, v6, s64, v250
	v_med3_f32 v7, v7, s64, v250
	v_med3_f32 v8, v8, s64, v250
	v_med3_f32 v9, v9, s64, v250
	v_med3_f32 v10, v10, s64, v250
	v_med3_f32 v11, v11, s64, v250
	v_cvt_pk_fp8_f32 v12, v4, v5
	v_cvt_pk_fp8_f32 v13, v8, v9
	s_nop 0
	v_cvt_pk_fp8_f32 v12, v6, v7 op_sel:[0,0,1]
	v_cvt_pk_fp8_f32 v13, v10, v11 op_sel:[0,0,1]
	v_add_u32_e32 v18, 0x80, v0
	v_mad_i64_i32 v[18:19], s[22:23], v18, s73, v[2:3]
	global_store_dwordx2 v[18:19], v[12:13], off
	v_pk_mul_f32 v[4:5], v[78:79], v[14:15] op_sel_hi:[1,0]
	v_pk_mul_f32 v[6:7], v[80:81], v[14:15] op_sel_hi:[1,0]
	v_pk_mul_f32 v[8:9], v[70:71], v[14:15] op_sel_hi:[1,0]
	v_pk_mul_f32 v[10:11], v[72:73], v[14:15] op_sel_hi:[1,0]
	v_exp_f32_e32 v4, v4
	v_exp_f32_e32 v5, v5
	v_exp_f32_e32 v6, v6
	v_exp_f32_e32 v7, v7
	v_exp_f32_e32 v8, v8
	v_exp_f32_e32 v9, v9
	v_exp_f32_e32 v10, v10
	v_exp_f32_e32 v11, v11
	v_pk_add_f32 v[4:5], v[4:5], v[20:21] op_sel_hi:[1,0]
	v_pk_add_f32 v[6:7], v[6:7], v[20:21] op_sel_hi:[1,0]
	v_pk_add_f32 v[8:9], v[8:9], v[20:21] op_sel_hi:[1,0]
	v_pk_add_f32 v[10:11], v[10:11], v[20:21] op_sel_hi:[1,0]
	v_rcp_f32_e32 v4, v4
	v_rcp_f32_e32 v5, v5
	v_rcp_f32_e32 v6, v6
	v_rcp_f32_e32 v7, v7
	v_rcp_f32_e32 v8, v8
	v_rcp_f32_e32 v9, v9
	v_rcp_f32_e32 v10, v10
	v_rcp_f32_e32 v11, v11
	v_pk_mul_f32 v[4:5], v[78:79], v[4:5]
	v_pk_mul_f32 v[6:7], v[80:81], v[6:7]
	v_pk_mul_f32 v[8:9], v[70:71], v[8:9]
	v_pk_mul_f32 v[10:11], v[72:73], v[10:11]
	v_pk_mul_f32 v[4:5], v[74:75], v[4:5]
	v_pk_mul_f32 v[6:7], v[76:77], v[6:7]
	v_pk_mul_f32 v[8:9], v[66:67], v[8:9]
; __device__ __forceinline__ u32x4 pack8(const f32x4 a, const f32x4 b) { u32x4 w; w.x = cvt_pk_bf16(a[0], a[1]); w.y = cvt_pk_bf16(a[2], a[3]); w.z = cvt_pk_bf16(b[0], b[1]); w.w = cvt_pk_bf16(b[2], b[3]); return w; }
; __device__ __forceinline__ float silu_f(float x) { return x * __builtin_amdgcn_rcpf(1.0f + __builtin_amdgcn_exp2f(-1.4426950409f * x)); }
;     w = __builtin_amdgcn_cvt_pk_fp8_f32(__builtin_amdgcn_fmed3f(v[2] * 8.0f, -448.0f, 448.0f), __builtin_amdgcn_fmed3f(v[3] * 8.0f, -448.0f, 448.0f), w, true); return (unsigned)w; }
;     __device__ __forceinline__ void operator()(const f32x4 (&acc)[2][2][4][2], const Unit& u, int wr, int wc, int fr, int fq) const {
;     ...
;         const int row0 = u.pm * BM + wr * 64 + fr, col0 = u.pn * HALF + wc * 32 + 8 * fq;
; #pragma unroll
;         for (int ai = 0; ai < 2; ++ai)
; #pragma unroll
;             for (int m = 0; m < 4; ++m) {
;                 const float r = rs[ai][m]; f32x4 o[2];
; #pragma unroll
;                 for (int n = 0; n < 2; ++n) { const f32x4 a = acc[ai][0][m][n] * r, b = acc[ai][1][m][n] * r;
;                     o[n] = (f32x4){silu_f(a[0]) * b[0], silu_f(a[1]) * b[1], silu_f(a[2]) * b[2], silu_f(a[3]) * b[3]}; }
;                 if (F8OUT) { u32x2 w; w.x = pack4_fp8(o[0]); w.y = pack4_fp8(o[1]); *(u32x2*)((unsigned char*)h + (size_t)(row0 + ai * HALF + m * 16) * FFN + col0) = w; }
;                 else *(u32x4*)(h + (size_t)(row0 + ai * HALF + m * 16) * FFN + col0) = pack8(o[0], o[1]);
;             }
; template <class Epi, class Sched, bool ALIGN_EPI = false, bool SP2 = false, bool F8 = false>
; __device__ __forceinline__ void gemm_phase(PG8_LAS unsigned char* lds, const Gemm g, const Sched& S, const Epi& E, const int tidb  ) {
;     ...
;         if constexpr (!Epi::AFTER_DRAIN) { E(acc, cur, wr, wc, fr, fq); S.done(cur); }
;         if (!has_next) break;
	v_pk_mul_f32 v[10:11], v[68:69], v[10:11]
	v_med3_f32 v4, v4, s64, v250
	v_med3_f32 v5, v5, s64, v250
	v_med3_f32 v6, v6, s64, v250
	v_med3_f32 v7, v7, s64, v250
	v_med3_f32 v8, v8, s64, v250
	v_med3_f32 v9, v9, s64, v250
	v_med3_f32 v10, v10, s64, v250
	v_med3_f32 v11, v11, s64, v250
	v_cvt_pk_fp8_f32 v12, v4, v5
	v_cvt_pk_fp8_f32 v13, v8, v9
	s_nop 0
	v_cvt_pk_fp8_f32 v12, v6, v7 op_sel:[0,0,1]
	v_cvt_pk_fp8_f32 v13, v10, v11 op_sel:[0,0,1]
	v_add_u32_e32 v18, 0x90, v0
	v_mad_i64_i32 v[18:19], s[22:23], v18, s73, v[2:3]
	global_store_dwordx2 v[18:19], v[12:13], off
	v_pk_mul_f32 v[4:5], v[62:63], v[14:15] op_sel_hi:[1,0]
	v_pk_mul_f32 v[6:7], v[64:65], v[14:15] op_sel_hi:[1,0]
	v_pk_mul_f32 v[8:9], v[54:55], v[14:15] op_sel_hi:[1,0]
	v_pk_mul_f32 v[10:11], v[56:57], v[14:15] op_sel_hi:[1,0]
	v_exp_f32_e32 v4, v4
	v_exp_f32_e32 v5, v5
	v_exp_f32_e32 v6, v6
	v_exp_f32_e32 v7, v7
	v_exp_f32_e32 v8, v8
	v_exp_f32_e32 v9, v9
	v_exp_f32_e32 v10, v10
	v_exp_f32_e32 v11, v11
	v_pk_add_f32 v[4:5], v[4:5], v[20:21] op_sel_hi:[1,0]
	v_pk_add_f32 v[6:7], v[6:7], v[20:21] op_sel_hi:[1,0]
	v_pk_add_f32 v[8:9], v[8:9], v[20:21] op_sel_hi:[1,0]
	v_pk_add_f32 v[10:11], v[10:11], v[20:21] op_sel_hi:[1,0]
	v_rcp_f32_e32 v4, v4
	v_rcp_f32_e32 v5, v5
	v_rcp_f32_e32 v6, v6
	v_rcp_f32_e32 v7, v7
	v_rcp_f32_e32 v8, v8
	v_rcp_f32_e32 v9, v9
	v_rcp_f32_e32 v10, v10
	v_rcp_f32_e32 v11, v11
	v_pk_mul_f32 v[4:5], v[62:63], v[4:5]
	v_pk_mul_f32 v[6:7], v[64:65], v[6:7]
	v_pk_mul_f32 v[8:9], v[54:55], v[8:9]
	v_pk_mul_f32 v[10:11], v[56:57], v[10:11]
	v_pk_mul_f32 v[4:5], v[58:59], v[4:5]
	v_pk_mul_f32 v[6:7], v[60:61], v[6:7]
	v_pk_mul_f32 v[8:9], v[50:51], v[8:9]
	v_pk_mul_f32 v[10:11], v[52:53], v[10:11]
	v_med3_f32 v4, v4, s64, v250
	v_med3_f32 v5, v5, s64, v250
	v_med3_f32 v6, v6, s64, v250
	v_med3_f32 v7, v7, s64, v250
	v_med3_f32 v8, v8, s64, v250
	v_med3_f32 v9, v9, s64, v250
	v_med3_f32 v10, v10, s64, v250
	v_med3_f32 v11, v11, s64, v250
	v_cvt_pk_fp8_f32 v12, v4, v5
	v_cvt_pk_fp8_f32 v13, v8, v9
	s_nop 0
	v_cvt_pk_fp8_f32 v12, v6, v7 op_sel:[0,0,1]
	v_cvt_pk_fp8_f32 v13, v10, v11 op_sel:[0,0,1]
	v_add_u32_e32 v18, 0xa0, v0
	v_mad_i64_i32 v[18:19], s[22:23], v18, s73, v[2:3]
	global_store_dwordx2 v[18:19], v[12:13], off
	v_pk_mul_f32 v[4:5], v[46:47], v[14:15] op_sel_hi:[1,0]
	v_pk_mul_f32 v[6:7], v[48:49], v[14:15] op_sel_hi:[1,0]
	v_pk_mul_f32 v[8:9], v[38:39], v[14:15] op_sel_hi:[1,0]
	v_pk_mul_f32 v[10:11], v[40:41], v[14:15] op_sel_hi:[1,0]
	v_exp_f32_e32 v4, v4
	v_exp_f32_e32 v5, v5
	v_exp_f32_e32 v6, v6
	v_exp_f32_e32 v7, v7
	v_exp_f32_e32 v8, v8
	v_exp_f32_e32 v9, v9
	v_exp_f32_e32 v10, v10
	v_exp_f32_e32 v11, v11
	v_pk_add_f32 v[4:5], v[4:5], v[20:21] op_sel_hi:[1,0]
	v_pk_add_f32 v[6:7], v[6:7], v[20:21] op_sel_hi:[1,0]
	v_pk_add_f32 v[8:9], v[8:9], v[20:21] op_sel_hi:[1,0]
	v_pk_add_f32 v[10:11], v[10:11], v[20:21] op_sel_hi:[1,0]
	v_rcp_f32_e32 v4, v4
	v_rcp_f32_e32 v5, v5
	v_rcp_f32_e32 v6, v6
	v_rcp_f32_e32 v7, v7
	v_rcp_f32_e32 v8, v8
	v_rcp_f32_e32 v9, v9
	v_rcp_f32_e32 v10, v10
	v_rcp_f32_e32 v11, v11
	v_pk_mul_f32 v[4:5], v[46:47], v[4:5]
	v_pk_mul_f32 v[6:7], v[48:49], v[6:7]
	v_pk_mul_f32 v[8:9], v[38:39], v[8:9]
	v_pk_mul_f32 v[10:11], v[40:41], v[10:11]
	v_pk_mul_f32 v[4:5], v[42:43], v[4:5]
	v_pk_mul_f32 v[6:7], v[44:45], v[6:7]
	v_pk_mul_f32 v[8:9], v[34:35], v[8:9]
	v_pk_mul_f32 v[10:11], v[36:37], v[10:11]
	v_med3_f32 v4, v4, s64, v250
	v_med3_f32 v5, v5, s64, v250
	v_med3_f32 v6, v6, s64, v250
	v_med3_f32 v7, v7, s64, v250
	v_med3_f32 v8, v8, s64, v250
	v_med3_f32 v9, v9, s64, v250
	v_med3_f32 v10, v10, s64, v250
	v_med3_f32 v11, v11, s64, v250
	v_cvt_pk_fp8_f32 v12, v4, v5
	v_cvt_pk_fp8_f32 v13, v8, v9
	s_nop 0
	v_cvt_pk_fp8_f32 v12, v6, v7 op_sel:[0,0,1]
	v_cvt_pk_fp8_f32 v13, v10, v11 op_sel:[0,0,1]
	v_add_u32_e32 v0, 0xb0, v0
	v_mad_i64_i32 v[2:3], s[22:23], v0, s73, v[2:3]
	s_mov_b64 s[22:23], -1
	s_and_b64 vcc, exec, s[2:3]
	global_store_dwordx2 v[2:3], v[12:13], off
	s_cbranch_vccnz .LBB0_1358
	s_andn2_b64 vcc, exec, s[14:15]
	s_cbranch_vccnz .LBB0_1357
	s_barrier
	s_branch .LBB0_1357
